# speedup vs baseline: 1.0146x; 1.0069x over previous
.LBB3_2:
	v_add_u32_e32 v206, s27, v214
	ds_read_b64_tr_b16 v[194:195], v206 offset:24576
	ds_read_b64_tr_b16 v[196:197], v206 offset:25088
	s_waitcnt lgkmcnt(9)
	v_mfma_f32_32x32x16_bf16 v[114:129], v[190:193], v[158:161], v[50:65]
	v_add_f32_e32 v98, v82, v83
	v_add_f32_e32 v98, v84, v98
	v_add_f32_e32 v98, v85, v98
	v_add_f32_e32 v98, v86, v98
	v_add_f32_e32 v130, v87, v98
	v_cvt_pk_bf16_f32 v142, v82, v83
	v_cvt_pk_bf16_f32 v143, v84, v85
	s_nop 0
	ds_read_b64_tr_b16 v[190:191], v206 offset:28672
	ds_read_b64_tr_b16 v[192:193], v206 offset:29184
	v_add_f32_e32 v82, v88, v130
	v_add_f32_e32 v82, v89, v82
	s_waitcnt lgkmcnt(10)
	v_mfma_f32_32x32x16_bf16 v[98:113], v[186:189], v[158:161], v[50:65]
	v_add_f32_e32 v82, v90, v82
	v_add_f32_e32 v82, v91, v82
	v_cvt_pk_bf16_f32 v144, v86, v87
	v_cvt_pk_bf16_f32 v145, v88, v89
	s_nop 0
	ds_read_b64_tr_b16 v[186:187], v206 offset:25600
	ds_read_b64_tr_b16 v[188:189], v206 offset:26112
	s_waitcnt lgkmcnt(11)
	v_mfma_f32_32x32x16_bf16 v[114:129], v[182:185], v[154:157], v[114:129]
	v_add_f32_e32 v82, v92, v82
	v_add_f32_e32 v82, v93, v82
	v_add_f32_e32 v82, v94, v82
	v_add_f32_e32 v82, v95, v82
	v_cvt_pk_bf16_f32 v138, v90, v91
	v_cvt_pk_bf16_f32 v139, v92, v93
	s_nop 0
	ds_read_b64_tr_b16 v[86:87], v206 offset:29696
	ds_read_b64_tr_b16 v[88:89], v206 offset:30208
	s_waitcnt lgkmcnt(12)
	v_mfma_f32_32x32x16_bf16 v[98:113], v[178:181], v[154:157], v[98:113]
	v_add_f32_e32 v82, v96, v82
	v_add_f32_e32 v82, v97, v82
	v_add_f32_e32 v82, v66, v82
	v_add_f32_e32 v90, v67, v82
	v_cvt_pk_bf16_f32 v140, v94, v95
	v_cvt_pk_bf16_f32 v141, v96, v97
	s_nop 0
	ds_read_b64_tr_b16 v[82:83], v206 offset:26624
	ds_read_b64_tr_b16 v[84:85], v206 offset:27136
	s_waitcnt lgkmcnt(13)
	v_mfma_f32_32x32x16_bf16 v[114:129], v[174:177], v[150:153], v[114:129]
	v_add_f32_e32 v90, v68, v90
	v_add_f32_e32 v90, v69, v90
	v_add_f32_e32 v90, v70, v90
	v_add_f32_e32 v90, v71, v90
	v_cvt_pk_bf16_f32 v134, v66, v67
	v_cvt_pk_bf16_f32 v135, v68, v69
	s_nop 0
	ds_read_b64_tr_b16 v[66:67], v206 offset:30720
	ds_read_b64_tr_b16 v[68:69], v206 offset:31232
	s_waitcnt lgkmcnt(14)
	v_mfma_f32_32x32x16_bf16 v[98:113], v[170:173], v[150:153], v[98:113]
	v_add_f32_e32 v90, v72, v90
	v_add_f32_e32 v90, v73, v90
	v_add_f32_e32 v90, v74, v90
	v_add_f32_e32 v90, v75, v90
	v_cvt_pk_bf16_f32 v136, v70, v71
	v_cvt_pk_bf16_f32 v137, v72, v73
	s_nop 0
	ds_read_b64_tr_b16 v[70:71], v206 offset:27648
	ds_read_b64_tr_b16 v[72:73], v206 offset:28160
	s_waitcnt lgkmcnt(14)
	v_mfma_f32_32x32x16_bf16 v[114:129], v[166:169], v[146:149], v[114:129]
	v_add_f32_e32 v90, v76, v90
	v_add_f32_e32 v90, v77, v90
	v_add_f32_e32 v90, v78, v90
	v_add_f32_e32 v90, v79, v90
	v_cvt_pk_bf16_f32 v130, v74, v75
	v_cvt_pk_bf16_f32 v131, v76, v77
	s_nop 0
	ds_read_b64_tr_b16 v[74:75], v206 offset:31744
	ds_read_b64_tr_b16 v[76:77], v206 offset:32256
	v_mfma_f32_32x32x16_bf16 v[98:113], v[162:165], v[146:149], v[98:113]
	v_add_f32_e32 v90, v80, v90
	v_add_f32_e32 v90, v81, v90
	v_add_f32_e32 v90, 0, v90
	v_cvt_pk_bf16_f32 v132, v78, v79
	v_cvt_pk_bf16_f32 v133, v80, v81
	s_nop 0
	v_lshl_add_u64 v[78:79], v[204:205], 0, s[24:25]
	s_add_i32 s26, s39, s35
	s_mov_b32 s27, m0
	s_mov_b32 m0, s26
	s_nop 0
	global_load_lds_dwordx4 v[78:79], off
	s_mov_b32 m0, s27
	v_max_f32_e32 v78, v115, v115
	v_max_f32_e32 v79, v114, v114
	v_max_f32_e32 v78, v79, v78
	s_nop 2
	v_max3_f32 v79, v116, v117, v99
	v_max3_f32 v78, v78, v98, v100
	v_max3_f32 v78, v78, v101, v118
	v_max3_f32 v79, v79, v120, v121
	v_max3_f32 v78, v78, v119, v102
	v_max3_f32 v79, v79, v104, v105
	v_max3_f32 v78, v78, v103, v122
	v_max3_f32 v79, v79, v124, v125
	v_max3_f32 v78, v78, v123, v106
	v_max3_f32 v79, v79, v108, v109
	v_max3_f32 v78, v78, v107, v126
	v_max3_f32 v79, v79, v128, v129
	v_max3_f32 v78, v78, v127, v110
	v_max3_f32 v79, v79, v112, v113
	v_max3_f32 v78, v78, v111, v79
	v_mov_b32_e32 v79, v78
	s_nop 1
	v_permlane32_swap_b32_e32 v78, v79
	v_max_f32_e32 v79, v79, v79
	v_max_f32_e32 v78, v78, v78
	v_max_f32_e32 v78, v78, v79
	v_lshl_add_u64 v[206:207], v[208:209], 0, s[18:19]
	s_add_i32 s26, s38, s34
	s_mov_b32 s27, m0
	s_mov_b32 m0, s26
	s_nop 0
	global_load_lds_dwordx4 v[206:207], off
	s_mov_b32 m0, s27
	v_cmp_lt_f32_e32 vcc, s15, v78
	s_cmp_lg_u64 vcc, 0
	v_add_f32_e32 v201, v201, v90
	s_cselect_b64 s[26:27], -1, 0
	s_cbranch_vccnz .LBB3_11

.LBB3_6:
	s_add_i32 s26, s38, 0x2000
	s_cmpk_lg_i32 s38, 0x4000
	s_cselect_b32 s40, s26, 0
	v_add_u32_e32 v217, s39, v214
	ds_read_b64_tr_b16 v[162:163], v217 offset:24576
	ds_read_b64_tr_b16 v[164:165], v217 offset:25088
	s_waitcnt lgkmcnt(9)
	v_mfma_f32_32x32x16_bf16 v[82:97], v[78:81], v[158:161], v[50:65]
	v_add_f32_e32 v66, v114, v115
	v_add_f32_e32 v66, v116, v66
	v_add_f32_e32 v66, v117, v66
	v_add_f32_e32 v66, v118, v66
	v_add_f32_e32 v66, v119, v66
	v_cvt_pk_bf16_f32 v142, v114, v115
	v_cvt_pk_bf16_f32 v143, v116, v117
	s_nop 0
	ds_read_b64_tr_b16 v[170:171], v217 offset:28672
	ds_read_b64_tr_b16 v[172:173], v217 offset:29184
	v_add_f32_e32 v66, v120, v66
	v_add_f32_e32 v66, v121, v66
	v_add_f32_e32 v66, v122, v66
	v_add_f32_e32 v114, v123, v66
	s_waitcnt lgkmcnt(10)
	v_mfma_f32_32x32x16_bf16 v[66:81], v[166:169], v[158:161], v[50:65]
	v_cvt_pk_bf16_f32 v144, v118, v119
	v_cvt_pk_bf16_f32 v145, v120, v121
	s_nop 0
	ds_read_b64_tr_b16 v[166:167], v217 offset:25600
	ds_read_b64_tr_b16 v[168:169], v217 offset:26112
	s_waitcnt lgkmcnt(11)
	v_mfma_f32_32x32x16_bf16 v[82:97], v[194:197], v[154:157], v[82:97]
	v_add_f32_e32 v114, v124, v114
	v_add_f32_e32 v114, v125, v114
	v_add_f32_e32 v114, v126, v114
	v_add_f32_e32 v114, v127, v114
	v_cvt_pk_bf16_f32 v138, v122, v123
	v_cvt_pk_bf16_f32 v139, v124, v125
	s_nop 0
	ds_read_b64_tr_b16 v[118:119], v217 offset:29696
	ds_read_b64_tr_b16 v[120:121], v217 offset:30208
	s_waitcnt lgkmcnt(12)
	v_mfma_f32_32x32x16_bf16 v[66:81], v[190:193], v[154:157], v[66:81]
	v_add_f32_e32 v114, v128, v114
	v_add_f32_e32 v114, v129, v114
	v_add_f32_e32 v114, v98, v114
	v_add_f32_e32 v122, v99, v114
	v_cvt_pk_bf16_f32 v140, v126, v127
	v_cvt_pk_bf16_f32 v141, v128, v129
	s_nop 0
	ds_read_b64_tr_b16 v[114:115], v217 offset:26624
	ds_read_b64_tr_b16 v[116:117], v217 offset:27136
	s_waitcnt lgkmcnt(13)
	v_mfma_f32_32x32x16_bf16 v[82:97], v[186:189], v[150:153], v[82:97]
	v_add_f32_e32 v122, v100, v122
	v_add_f32_e32 v122, v101, v122
	v_add_f32_e32 v122, v102, v122
	v_add_f32_e32 v122, v103, v122
	v_cvt_pk_bf16_f32 v134, v98, v99
	v_cvt_pk_bf16_f32 v135, v100, v101
	s_nop 0
	ds_read_b64_tr_b16 v[98:99], v217 offset:30720
	ds_read_b64_tr_b16 v[100:101], v217 offset:31232
	s_waitcnt lgkmcnt(14)
	v_mfma_f32_32x32x16_bf16 v[66:81], v[178:181], v[150:153], v[66:81]
	v_add_f32_e32 v122, v104, v122
	v_add_f32_e32 v122, v105, v122
	v_add_f32_e32 v122, v106, v122
	v_add_f32_e32 v122, v107, v122
	v_cvt_pk_bf16_f32 v136, v102, v103
	v_cvt_pk_bf16_f32 v137, v104, v105
	s_nop 0
	ds_read_b64_tr_b16 v[102:103], v217 offset:27648
	ds_read_b64_tr_b16 v[104:105], v217 offset:28160
	s_waitcnt lgkmcnt(14)
	v_mfma_f32_32x32x16_bf16 v[82:97], v[182:185], v[146:149], v[82:97]
	v_add_f32_e32 v122, v108, v122
	v_add_f32_e32 v122, v109, v122
	v_add_f32_e32 v122, v110, v122
	v_add_f32_e32 v122, v111, v122
	v_cvt_pk_bf16_f32 v130, v106, v107
	v_cvt_pk_bf16_f32 v131, v108, v109
	s_nop 0
	ds_read_b64_tr_b16 v[106:107], v217 offset:31744
	ds_read_b64_tr_b16 v[108:109], v217 offset:32256
	v_mfma_f32_32x32x16_bf16 v[66:81], v[174:177], v[146:149], v[66:81]
	v_add_f32_e32 v122, v112, v122
	v_add_f32_e32 v122, v113, v122
	v_add_f32_e32 v122, 0, v122
	v_cvt_pk_bf16_f32 v132, v110, v111
	v_cvt_pk_bf16_f32 v133, v112, v113
	s_nop 0
	v_lshl_add_u64 v[110:111], v[204:205], 0, s[20:21]
	s_add_i32 s26, s38, s35
	s_mov_b32 s27, m0
	s_mov_b32 m0, s26
	s_nop 0
	global_load_lds_dwordx4 v[110:111], off
	s_mov_b32 m0, s27
	v_lshl_add_u64 v[110:111], v[208:209], 0, s[16:17]
	s_add_i32 s26, s40, s34
	s_mov_b32 s27, m0
	s_mov_b32 m0, s26
	s_nop 0
	global_load_lds_dwordx4 v[110:111], off
	s_mov_b32 m0, s27
	v_max_f32_e32 v110, v83, v83
	v_max_f32_e32 v111, v82, v82
	v_max_f32_e32 v110, v111, v110
	s_nop 0
	v_max3_f32 v111, v84, v85, v67
	v_max3_f32 v110, v110, v66, v68
	v_max3_f32 v110, v110, v69, v86
	v_max3_f32 v111, v111, v88, v89
	v_max3_f32 v110, v110, v87, v70
	v_max3_f32 v111, v111, v72, v73
	v_max3_f32 v110, v110, v71, v90
	v_max3_f32 v111, v111, v92, v93
	v_max3_f32 v110, v110, v91, v74
	v_max3_f32 v111, v111, v76, v77
	v_max3_f32 v110, v110, v75, v94
	v_max3_f32 v111, v111, v96, v97
	v_max3_f32 v110, v110, v95, v78
	v_max3_f32 v111, v111, v80, v81
	v_max3_f32 v110, v110, v79, v111
	v_mov_b32_e32 v111, v110
	s_nop 1
	v_permlane32_swap_b32_e32 v110, v111
	v_max_f32_e32 v111, v111, v111
	v_max_f32_e32 v110, v110, v110
	v_max_f32_e32 v110, v110, v111
	v_cmp_lt_f32_e32 vcc, s15, v110
	s_cmp_lg_u64 vcc, 0
	v_add_f32_e32 v201, v201, v122
	s_cselect_b64 s[26:27], -1, 0
	s_cbranch_vccnz .LBB3_14

.LBB3_17:
	v_mov_b64_e32 v[34:35], v[50:51]
	v_mov_b64_e32 v[36:37], v[52:53]
	v_mov_b64_e32 v[38:39], v[54:55]
	v_mov_b64_e32 v[40:41], v[56:57]
	v_mov_b64_e32 v[42:43], v[58:59]
	v_mov_b64_e32 v[44:45], v[60:61]
	v_mov_b64_e32 v[46:47], v[62:63]
	v_mov_b64_e32 v[48:49], v[64:65]
	ds_read_b64_tr_b16 v[114:115], v214 offset:40960
	ds_read_b64_tr_b16 v[116:117], v214 offset:41472
	s_waitcnt lgkmcnt(9)
	v_mfma_f32_32x32x16_bf16 v[98:113], v[190:193], v[158:161], v[34:49]
	v_add_f32_e32 v50, v82, v83
	v_add_f32_e32 v50, v84, v50
	v_add_f32_e32 v50, v85, v50
	v_add_f32_e32 v50, v86, v50
	v_add_f32_e32 v50, v87, v50
	v_cvt_pk_bf16_f32 v142, v82, v83
	v_cvt_pk_bf16_f32 v143, v84, v85
	s_nop 0
	ds_read_b64_tr_b16 v[122:123], v214 offset:45056
	ds_read_b64_tr_b16 v[124:125], v214 offset:45568
	v_add_f32_e32 v50, v88, v50
	v_add_f32_e32 v50, v89, v50
	v_add_f32_e32 v50, v90, v50
	v_add_f32_e32 v82, v91, v50
	s_waitcnt lgkmcnt(10)
	v_mfma_f32_32x32x16_bf16 v[50:65], v[186:189], v[158:161], v[34:49]
	v_cvt_pk_bf16_f32 v144, v86, v87
	v_cvt_pk_bf16_f32 v145, v88, v89
	s_nop 0
	ds_read_b64_tr_b16 v[118:119], v214 offset:41984
	ds_read_b64_tr_b16 v[120:121], v214 offset:42496
	s_waitcnt lgkmcnt(11)
	v_mfma_f32_32x32x16_bf16 v[98:113], v[182:185], v[154:157], v[98:113]
	v_add_f32_e32 v82, v92, v82
	v_add_f32_e32 v82, v93, v82
	v_add_f32_e32 v82, v94, v82
	v_add_f32_e32 v82, v95, v82
	v_cvt_pk_bf16_f32 v138, v90, v91
	v_cvt_pk_bf16_f32 v139, v92, v93
	s_nop 0
	ds_read_b64_tr_b16 v[86:87], v214 offset:46080
	ds_read_b64_tr_b16 v[88:89], v214 offset:46592
	s_waitcnt lgkmcnt(12)
	v_mfma_f32_32x32x16_bf16 v[50:65], v[178:181], v[154:157], v[50:65]
	v_add_f32_e32 v82, v96, v82
	v_add_f32_e32 v82, v97, v82
	v_add_f32_e32 v82, v66, v82
	v_add_f32_e32 v90, v67, v82
	v_cvt_pk_bf16_f32 v140, v94, v95
	v_cvt_pk_bf16_f32 v141, v96, v97
	s_nop 0
	ds_read_b64_tr_b16 v[82:83], v214 offset:43008
	ds_read_b64_tr_b16 v[84:85], v214 offset:43520
	s_waitcnt lgkmcnt(13)
	v_mfma_f32_32x32x16_bf16 v[98:113], v[174:177], v[150:153], v[98:113]
	v_add_f32_e32 v90, v68, v90
	v_add_f32_e32 v90, v69, v90
	v_add_f32_e32 v90, v70, v90
	v_add_f32_e32 v90, v71, v90
	v_cvt_pk_bf16_f32 v134, v66, v67
	v_cvt_pk_bf16_f32 v135, v68, v69
	s_nop 0
	ds_read_b64_tr_b16 v[66:67], v214 offset:47104
	ds_read_b64_tr_b16 v[68:69], v214 offset:47616
	s_waitcnt lgkmcnt(14)
	v_mfma_f32_32x32x16_bf16 v[50:65], v[170:173], v[150:153], v[50:65]
	v_add_f32_e32 v90, v72, v90
	v_add_f32_e32 v90, v73, v90
	v_add_f32_e32 v90, v74, v90
	v_add_f32_e32 v90, v75, v90
	v_cvt_pk_bf16_f32 v136, v70, v71
	v_cvt_pk_bf16_f32 v137, v72, v73
	s_nop 0
	ds_read_b64_tr_b16 v[70:71], v214 offset:44032
	ds_read_b64_tr_b16 v[72:73], v214 offset:44544
	s_waitcnt lgkmcnt(14)
	v_mfma_f32_32x32x16_bf16 v[98:113], v[166:169], v[146:149], v[98:113]
	v_add_f32_e32 v90, v76, v90
	v_add_f32_e32 v90, v77, v90
	v_add_f32_e32 v90, v78, v90
	v_add_f32_e32 v90, v79, v90
	v_cvt_pk_bf16_f32 v130, v74, v75
	v_cvt_pk_bf16_f32 v131, v76, v77
	s_nop 0
	ds_read_b64_tr_b16 v[74:75], v214 offset:48128
	ds_read_b64_tr_b16 v[76:77], v214 offset:48640
	v_mfma_f32_32x32x16_bf16 v[50:65], v[162:165], v[146:149], v[50:65]
	v_add_f32_e32 v90, v80, v90
	v_add_f32_e32 v90, v81, v90
	v_add_f32_e32 v90, 0, v90
	v_cvt_pk_bf16_f32 v132, v78, v79
	v_cvt_pk_bf16_f32 v133, v80, v81
	s_nop 0
	v_mov_b32_e32 v78, 0xf00
	v_mad_i64_i32 v[186:187], s[14:15], s14, v78, v[202:203]
	v_mov_b32_e32 v78, 0xe00
	s_mov_b32 s11, m0
	s_mov_b32 m0, s35
	s_nop 0
	global_load_lds_dwordx4 v[186:187], off
	s_mov_b32 m0, s11
	v_mad_i64_i32 v[78:79], s[14:15], s10, v78, v[198:199]
	s_mov_b32 s11, m0
	s_mov_b32 m0, s33
	s_nop 0
	global_load_lds_dwordx4 v[78:79], off
	s_mov_b32 m0, s11
	v_max_f32_e32 v78, v99, v99
	v_max_f32_e32 v79, v98, v98
	v_max_f32_e32 v78, v79, v78
	s_nop 0
	v_max3_f32 v79, v100, v101, v51
	v_max3_f32 v78, v78, v50, v52
	v_max3_f32 v78, v78, v53, v102
	v_max3_f32 v79, v79, v104, v105
	v_max3_f32 v78, v78, v103, v54
	v_max3_f32 v79, v79, v56, v57
	v_max3_f32 v78, v78, v55, v106
	v_max3_f32 v79, v79, v108, v109
	v_max3_f32 v78, v78, v107, v58
	v_max3_f32 v79, v79, v60, v61
	v_max3_f32 v78, v78, v59, v110
	v_max3_f32 v79, v79, v112, v113
	v_max3_f32 v78, v78, v111, v62
	v_max3_f32 v79, v79, v64, v65
	v_max3_f32 v78, v78, v63, v79
	v_mov_b32_e32 v79, v78
	s_nop 1
	v_permlane32_swap_b32_e32 v78, v79
	v_max_f32_e32 v79, v79, v79
	v_max_f32_e32 v78, v78, v78
	v_max_f32_e32 v78, v78, v79
	s_mov_b32 s11, 0x41000000
	v_cmp_lt_f32_e32 vcc, s11, v78
	s_cmp_lg_u64 vcc, 0
	v_add_f32_e32 v189, v201, v90
	s_cselect_b64 s[14:15], -1, 0
	s_cbranch_vccnz .LBB3_394

.LBB3_393:
	s_endpgm
	s_nop 0
	s_nop 0
	s_nop 0
	s_nop 0
	s_nop 0
	s_nop 0
	s_nop 0
	s_nop 0
	s_nop 0
	s_nop 0
	s_nop 0
	s_nop 0
	s_nop 0
	s_nop 0
	s_nop 0
	s_nop 0
	s_nop 0
	s_nop 0
	s_nop 0
	s_nop 0
	s_nop 0
	s_nop 0
	s_nop 0
	s_nop 0
	s_nop 0
	s_nop 0
	s_nop 0
	s_nop 0
	s_nop 0
	s_nop 0
	s_nop 0
	s_nop 0
